# P6 row RMS: 64-lane sum of squares via DPP adds + permlane16/32 swaps instead of six serial ds_bpermute round trips per row (on top of the NA last-tile change)
# baseline (speedup 1.0000x reference)
.LBB0_973:
	s_waitcnt vmcnt(15)
	v_and_b32_e32 v203, 0xffff0000, v133
	v_and_b32_e32 v201, 0xffff0000, v132
	v_lshlrev_b32_e32 v202, 16, v133
	v_mul_f32_e32 v130, v203, v203
	v_lshlrev_b32_e32 v200, 16, v132
	v_pk_fma_f32 v[168:169], v[202:203], v[202:203], v[130:131] op_sel_hi:[1,1,0]
	s_waitcnt vmcnt(14)
	v_and_b32_e32 v207, 0xffff0000, v135
	v_and_b32_e32 v206, 0xffff0000, v134
	v_mul_f32_e32 v130, v201, v201
	v_lshlrev_b32_e32 v205, 16, v135
	v_lshlrev_b32_e32 v204, 16, v134
	v_pk_mul_f32 v[170:171], v[206:207], v[206:207]
	s_waitcnt vmcnt(12)
	v_lshlrev_b32_e32 v213, 16, v144
	v_pk_fma_f32 v[172:173], v[200:201], v[200:201], v[130:131] op_sel_hi:[1,1,0]
	v_pk_fma_f32 v[170:171], v[204:205], v[204:205], v[170:171]
	v_and_b32_e32 v215, 0xffff0000, v144
	v_mov_b32_e32 v212, v172
	v_mov_b32_e32 v174, v168
	s_waitcnt lgkmcnt(0)
	v_mov_b32_e32 v175, v213
	v_and_b32_e32 v209, 0xffff0000, v140
	v_mul_f32_e32 v129, v215, v215
	v_pk_add_f32 v[168:169], v[172:173], v[168:169]
	v_pk_mul_f32 v[172:173], v[212:213], v[174:175]
	v_pk_add_f32 v[170:171], v[170:171], v[170:171] op_sel:[0,1] op_sel_hi:[1,0]
	v_lshlrev_b32_e32 v208, 16, v140
	v_and_b32_e32 v211, 0xffff0000, v141
	v_mov_b32_e32 v169, v173
	v_mov_b32_e32 v171, v129
	v_mul_f32_e32 v130, v209, v209
	v_lshlrev_b32_e32 v210, 16, v141
	v_lshlrev_b32_e32 v216, 16, v145
	v_and_b32_e32 v217, 0xffff0000, v145
	v_pk_add_f32 v[168:169], v[168:169], v[170:171]
	v_pk_fma_f32 v[170:171], v[208:209], v[208:209], v[130:131] op_sel_hi:[1,1,0]
	v_mul_f32_e32 v130, v211, v211
	v_mul_f32_e32 v176, v216, v216
	v_mul_f32_e32 v177, v217, v217
	v_pk_fma_f32 v[172:173], v[210:211], v[210:211], v[130:131] op_sel_hi:[1,1,0]
	v_mov_b32_e32 v171, v176
	v_mov_b32_e32 v173, v177
	v_pk_add_f32 v[170:171], v[170:171], v[172:173]
	s_waitcnt vmcnt(7)
	v_and_b32_e32 v221, 0xffff0000, v151
	v_and_b32_e32 v220, 0xffff0000, v150
	v_pk_add_f32 v[218:219], v[168:169], v[170:171]
	v_lshlrev_b32_e32 v177, 16, v151
	v_lshlrev_b32_e32 v176, 16, v150
	v_pk_mul_f32 v[168:169], v[220:221], v[220:221]
	s_waitcnt vmcnt(6)
	v_and_b32_e32 v181, 0xffff0000, v153
	v_pk_fma_f32 v[168:169], v[176:177], v[176:177], v[168:169]
	v_and_b32_e32 v180, 0xffff0000, v152
	v_pk_add_f32 v[222:223], v[168:169], v[168:169] op_sel:[0,1] op_sel_hi:[1,0]
	s_waitcnt vmcnt(4)
	v_lshlrev_b32_e32 v175, 16, v162
	v_pk_add_f32 v[218:219], v[218:219], v[218:219] op_sel:[0,1] op_sel_hi:[1,0]
	v_lshlrev_b32_e32 v183, 16, v153
	v_lshlrev_b32_e32 v182, 16, v152
	v_pk_mul_f32 v[168:169], v[180:181], v[180:181]
	v_mov_b32_e32 v174, v218
	v_mov_b32_e32 v226, v222
	v_mov_b32_e32 v227, v175
	v_pk_fma_f32 v[224:225], v[182:183], v[182:183], v[168:169]
	v_and_b32_e32 v173, 0xffff0000, v162
	v_pk_add_f32 v[218:219], v[218:219], v[222:223]
	v_pk_mul_f32 v[222:223], v[174:175], v[226:227]
	v_and_b32_e32 v171, 0xffff0000, v156
	v_mul_f32_e32 v129, v173, v173
	v_mov_b32_e32 v219, v223
	v_pk_add_f32 v[222:223], v[224:225], v[224:225] op_sel:[0,1] op_sel_hi:[1,0]
	v_lshlrev_b32_e32 v170, 16, v156
	v_and_b32_e32 v179, 0xffff0000, v157
	v_mov_b32_e32 v223, v129
	v_mul_f32_e32 v130, v171, v171
	v_lshlrev_b32_e32 v178, 16, v157
	v_lshlrev_b32_e32 v168, 16, v163
	v_and_b32_e32 v169, 0xffff0000, v163
	v_pk_add_f32 v[218:219], v[218:219], v[222:223]
	v_pk_fma_f32 v[222:223], v[170:171], v[170:171], v[130:131] op_sel_hi:[1,1,0]
	v_mul_f32_e32 v130, v179, v179
	v_mul_f32_e32 v172, v168, v168
	v_mul_f32_e32 v212, v169, v169
	v_pk_fma_f32 v[224:225], v[178:179], v[178:179], v[130:131] op_sel_hi:[1,1,0]
	v_mov_b32_e32 v223, v172
	v_mov_b32_e32 v225, v212
	v_pk_add_f32 v[222:223], v[222:223], v[224:225]
	s_nop 0
	v_pk_add_f32 v[218:219], v[218:219], v[222:223]
	s_barrier
	v_add_f32_e32 v129, v218, v219
	s_nop 1
	v_mov_b32_e32 v218, v205
	v_mov_b32_e32 v205, v206
	v_mov_b32_e32 v219, v207
	v_add_f32_dpp v129, v129, v129 quad_perm:[1,0,3,2] row_mask:0xf bank_mask:0xf
	s_nop 1
	v_and_b32_e32 v223, 0xffff0000, v142
	v_lshlrev_b32_e32 v224, 16, v143
	v_and_b32_e32 v225, 0xffff0000, v143
	v_mul_f32_e32 v222, v225, v225
	v_add_f32_dpp v129, v129, v129 quad_perm:[2,3,0,1] row_mask:0xf bank_mask:0xf
	s_nop 1
	v_and_b32_e32 v229, 0xffff0000, v147
	v_and_b32_e32 v228, 0xffff0000, v146
	s_waitcnt vmcnt(2)
	v_and_b32_e32 v233, 0xffff0000, v155
	v_and_b32_e32 v232, 0xffff0000, v154
	v_add_f32_dpp v129, v129, v129 row_half_mirror row_mask:0xf bank_mask:0xf
	s_nop 1
	s_waitcnt vmcnt(0)
	v_lshlrev_b32_e32 v239, 16, v160
	v_lshlrev_b32_e32 v231, 16, v155
	v_lshlrev_b32_e32 v230, 16, v154
	v_mov_b32_e32 v245, v239
	v_add_f32_dpp v129, v129, v129 row_mirror row_mask:0xf bank_mask:0xf
	v_mov_b32_e32 v130, v129
	v_and_b32_e32 v241, 0xffff0000, v160
	v_and_b32_e32 v235, 0xffff0000, v158
	v_lshlrev_b32_e32 v234, 16, v158
	v_and_b32_e32 v237, 0xffff0000, v159
	s_nop 1
	v_permlane16_swap_b32_e32 v129, v130
	v_add_f32_e32 v129, v129, v130
	v_mov_b32_e32 v130, v129
	v_lshlrev_b32_e32 v236, 16, v159
	v_lshlrev_b32_e32 v242, 16, v161
	v_and_b32_e32 v243, 0xffff0000, v161
	v_mov_b32_e32 v240, v239
	s_waitcnt lgkmcnt(0)
	s_nop 1
	v_permlane32_swap_b32_e32 v129, v130
	v_add_f32_e32 v129, v129, v130
	v_fmamk_f32 v129, v129, 0x3a000000, v193
	v_mul_f32_e32 v130, 0x4f800000, v129
	v_cmp_gt_f32_e32 vcc, s40, v129
	s_add_i32 s30, s30, s74
	s_cmpk_gt_i32 s30, 0x7ff
	v_cndmask_b32_e32 v129, v129, v130, vcc
	v_sqrt_f32_e32 v130, v129
	s_cselect_b64 s[34:35], -1, 0
	v_add_u32_e32 v172, -1, v130
	v_fma_f32 v174, -v172, v130, v129
	v_cmp_ge_f32_e64 s[12:13], 0, v174
	v_add_u32_e32 v174, 1, v130
	s_nop 0
	v_cndmask_b32_e64 v172, v130, v172, s[12:13]
	v_fma_f32 v130, -v174, v130, v129
	v_cmp_lt_f32_e64 s[12:13], 0, v130
	s_nop 1
	v_cndmask_b32_e64 v130, v172, v174, s[12:13]
	v_mul_f32_e32 v172, 0x37800000, v130
	v_cndmask_b32_e32 v130, v130, v172, vcc
	v_cmp_class_f32_e32 vcc, v129, v194
	s_nop 1
	v_cndmask_b32_e32 v129, v130, v129, vcc
	v_div_scale_f32 v130, s[12:13], v129, v129, 1.0
	v_rcp_f32_e32 v172, v130
	s_nop 0
	v_fma_f32 v174, -v130, v172, 1.0
	v_fmac_f32_e32 v172, v174, v172
	v_div_scale_f32 v174, vcc, 1.0, v129, 1.0
	v_mul_f32_e32 v212, v174, v172
	v_fma_f32 v214, -v130, v212, v174
	v_fmac_f32_e32 v212, v214, v172
	v_fma_f32 v130, -v130, v212, v174
	v_div_fmas_f32 v130, v130, v172, v212
	v_div_fixup_f32 v130, v130, v129, 1.0
	v_pk_mul_f32 v[204:205], v[130:131], v[204:205] op_sel_hi:[0,1]
	v_mov_b32_e32 v172, 0
	v_cvt_pk_fp8_f32 v172, v204, v205
	v_pk_mul_f32 v[200:201], v[130:131], v[200:201] op_sel_hi:[0,1]
	v_mov_b32_e32 v129, 0
	v_pk_mul_f32 v[206:207], v[130:131], v[218:219] op_sel_hi:[0,1]
	v_cvt_pk_fp8_f32 v129, v200, v201
	v_cvt_pk_fp8_f32 v172, v206, v207 op_sel:[0,0,1]
	v_pk_mul_f32 v[202:203], v[130:131], v[202:203] op_sel_hi:[0,1]
	v_mov_b32_e32 v214, v213
	v_cvt_pk_fp8_f32 v129, v202, v203 op_sel:[0,0,1]
	ds_write_b128 v195, v[200:203]
	global_store_dword v[166:167], v172, off offset:-1792
	v_pk_mul_f32 v[200:201], v[130:131], v[208:209] op_sel_hi:[0,1]
	v_pk_mul_f32 v[208:209], v[214:215], v[130:131] op_sel_hi:[1,0]
	v_mov_b32_e32 v172, 0
	v_cvt_pk_fp8_f32 v172, v208, v209
	global_store_dword v[166:167], v129, off offset:-2048
	v_mov_b32_e32 v129, 0
	v_pk_mul_f32 v[202:203], v[130:131], v[210:211] op_sel_hi:[0,1]
	v_pk_mul_f32 v[210:211], v[216:217], v[130:131] op_sel_hi:[1,0]
	v_cvt_pk_fp8_f32 v129, v200, v201
	v_cvt_pk_fp8_f32 v172, v210, v211 op_sel:[0,0,1]
	ds_write_b128 v195, v[208:211] offset:3072
	v_and_b32_e32 v211, 0xffff0000, v149
	v_cvt_pk_fp8_f32 v129, v202, v203 op_sel:[0,0,1]
	ds_write_b128 v195, v[200:203] offset:2048
	global_store_dword v[166:167], v172, off offset:-1280
	v_mov_b32_e32 v200, v177
	v_mov_b32_e32 v201, v221
	v_and_b32_e32 v209, 0xffff0000, v148
	v_lshlrev_b32_e32 v210, 16, v149
	v_mul_f32_e32 v172, v211, v211
	v_pk_mul_f32 v[202:203], v[130:131], v[200:201] op_sel_hi:[0,1]
	v_lshlrev_b32_e32 v208, 16, v148
	v_pk_fma_f32 v[200:201], v[210:211], v[210:211], v[172:173] op_sel_hi:[1,1,0]
	v_and_b32_e32 v215, 0xffff0000, v137
	v_and_b32_e32 v214, 0xffff0000, v136
	v_mul_f32_e32 v172, v209, v209
	ds_write_b128 v195, v[204:207] offset:1024
	v_lshlrev_b32_e32 v213, 16, v137
	v_lshlrev_b32_e32 v212, 16, v136
	v_pk_mul_f32 v[204:205], v[214:215], v[214:215]
	v_lshlrev_b32_e32 v221, 16, v142
	v_pk_fma_f32 v[206:207], v[208:209], v[208:209], v[172:173] op_sel_hi:[1,1,0]
	v_mov_b32_e32 v177, v220
	v_pk_fma_f32 v[204:205], v[212:213], v[212:213], v[204:205]
	v_mov_b32_e32 v220, v206
	v_mov_b32_e32 v226, v200
	v_mov_b32_e32 v227, v221
	global_store_dword v[166:167], v129, off offset:-1536
	v_and_b32_e32 v217, 0xffff0000, v138
	v_mul_f32_e32 v129, v223, v223
	v_pk_add_f32 v[200:201], v[206:207], v[200:201]
	v_pk_mul_f32 v[206:207], v[220:221], v[226:227]
	v_pk_add_f32 v[204:205], v[204:205], v[204:205] op_sel:[0,1] op_sel_hi:[1,0]
	v_lshlrev_b32_e32 v216, 16, v138
	v_and_b32_e32 v219, 0xffff0000, v139
	v_mov_b32_e32 v201, v207
	v_mov_b32_e32 v205, v129
	v_mul_f32_e32 v172, v217, v217
	v_lshlrev_b32_e32 v218, 16, v139
	v_pk_add_f32 v[200:201], v[200:201], v[204:205]
	v_pk_fma_f32 v[204:205], v[216:217], v[216:217], v[172:173] op_sel_hi:[1,1,0]
	v_mul_f32_e32 v172, v219, v219
	v_mul_f32_e32 v174, v224, v224
	v_pk_fma_f32 v[206:207], v[218:219], v[218:219], v[172:173] op_sel_hi:[1,1,0]
	v_mov_b32_e32 v205, v174
	v_mov_b32_e32 v207, v222
	v_pk_add_f32 v[204:205], v[204:205], v[206:207]
	v_lshlrev_b32_e32 v227, 16, v147
	v_pk_add_f32 v[200:201], v[200:201], v[204:205]
	v_lshlrev_b32_e32 v226, 16, v146
	v_pk_mul_f32 v[204:205], v[228:229], v[228:229]
	v_pk_add_f32 v[200:201], v[200:201], v[200:201] op_sel:[0,1] op_sel_hi:[1,0]
	v_pk_fma_f32 v[204:205], v[226:227], v[226:227], v[204:205]
	v_pk_mul_f32 v[206:207], v[232:233], v[232:233]
	v_pk_add_f32 v[204:205], v[204:205], v[204:205] op_sel:[0,1] op_sel_hi:[1,0]
	v_mov_b32_e32 v238, v200
	v_mov_b32_e32 v244, v204
	v_pk_fma_f32 v[206:207], v[230:231], v[230:231], v[206:207]
	v_pk_add_f32 v[200:201], v[200:201], v[204:205]
	v_pk_mul_f32 v[204:205], v[238:239], v[244:245]
	v_mul_f32_e32 v129, v241, v241
	v_mov_b32_e32 v201, v205
	v_pk_add_f32 v[204:205], v[206:207], v[206:207] op_sel:[0,1] op_sel_hi:[1,0]
	v_mul_f32_e32 v172, v235, v235
	v_mov_b32_e32 v205, v129
	v_pk_add_f32 v[200:201], v[200:201], v[204:205]
	v_pk_fma_f32 v[204:205], v[234:235], v[234:235], v[172:173] op_sel_hi:[1,1,0]
	v_mul_f32_e32 v172, v237, v237
	v_mul_f32_e32 v174, v242, v242
	v_mul_f32_e32 v220, v243, v243
	v_pk_fma_f32 v[206:207], v[236:237], v[236:237], v[172:173] op_sel_hi:[1,1,0]
	v_mov_b32_e32 v205, v174
	v_mov_b32_e32 v207, v220
	v_pk_add_f32 v[204:205], v[204:205], v[206:207]
	v_mov_b32_e32 v174, 0
	v_pk_add_f32 v[200:201], v[200:201], v[204:205]
	v_pk_mul_f32 v[178:179], v[130:131], v[178:179] op_sel_hi:[0,1]
	v_add_f32_e32 v129, v200, v201
	s_nop 1
	v_pk_mul_f32 v[200:201], v[130:131], v[176:177] op_sel_hi:[0,1]
	v_mov_b32_e32 v176, v183
	v_mov_b32_e32 v183, v180
	v_pk_mul_f32 v[204:205], v[130:131], v[182:183] op_sel_hi:[0,1]
	v_add_f32_dpp v129, v129, v129 quad_perm:[1,0,3,2] row_mask:0xf bank_mask:0xf
	s_nop 1
	v_mov_b32_e32 v180, 0
	v_cvt_pk_fp8_f32 v180, v204, v205
	v_mov_b32_e32 v177, v181
	v_pk_mul_f32 v[206:207], v[130:131], v[176:177] op_sel_hi:[0,1]
	v_add_f32_dpp v129, v129, v129 quad_perm:[2,3,0,1] row_mask:0xf bank_mask:0xf
	s_nop 1
	v_cvt_pk_fp8_f32 v180, v206, v207 op_sel:[0,0,1]
	v_pk_mul_f32 v[176:177], v[130:131], v[170:171] op_sel_hi:[0,1]
	v_cvt_pk_fp8_f32 v174, v200, v201
	ds_write_b128 v195, v[176:179] offset:6144
	v_add_f32_dpp v129, v129, v129 row_half_mirror row_mask:0xf bank_mask:0xf
	s_nop 1
	global_store_dword v[166:167], v180, off offset:-768
	v_cvt_pk_fp8_f32 v174, v202, v203 op_sel:[0,0,1]
	v_mov_b32_e32 v222, v221
	ds_write_b128 v195, v[200:203] offset:4096
	v_add_f32_dpp v129, v129, v129 row_mirror row_mask:0xf bank_mask:0xf
	v_mov_b32_e32 v172, v129
	global_store_dword v[166:167], v174, off offset:-1024
	v_mov_b32_e32 v174, 0
	v_cvt_pk_fp8_f32 v174, v176, v177
	ds_write_b128 v195, v[204:207] offset:5120
	s_nop 1
	v_permlane16_swap_b32_e32 v129, v172
	v_add_f32_e32 v129, v129, v172
	v_mov_b32_e32 v180, v129
	v_mov_b32_e32 v172, v175
	v_pk_mul_f32 v[170:171], v[172:173], v[130:131] op_sel_hi:[1,0]
	v_mov_b32_e32 v175, 0
	v_cvt_pk_fp8_f32 v175, v170, v171
	s_waitcnt lgkmcnt(0)
	s_nop 1
	v_permlane32_swap_b32_e32 v129, v180
	v_add_f32_e32 v129, v129, v180
	v_fmamk_f32 v129, v129, 0x3a000000, v193
	v_mul_f32_e32 v172, 0x4f800000, v129
	v_cmp_gt_f32_e32 vcc, s40, v129
	v_cvt_pk_fp8_f32 v174, v178, v179 op_sel:[0,0,1]
	v_mov_b32_e32 v182, 0
	v_cndmask_b32_e32 v129, v129, v172, vcc
	v_sqrt_f32_e32 v180, v129
	v_pk_mul_f32 v[172:173], v[168:169], v[130:131] op_sel_hi:[1,0]
	global_store_dword v[166:167], v174, off offset:-512
	v_cvt_pk_fp8_f32 v175, v172, v173 op_sel:[0,0,1]
	v_add_u32_e32 v130, -1, v180
	v_fma_f32 v168, -v130, v180, v129
	v_cmp_ge_f32_e64 s[12:13], 0, v168
	v_add_u32_e32 v168, 1, v180
	v_fma_f32 v169, -v168, v180, v129
	v_cndmask_b32_e64 v130, v180, v130, s[12:13]
	v_cmp_lt_f32_e64 s[12:13], 0, v169
	global_store_dword v[166:167], v175, off offset:-256
	ds_write_b128 v195, v[170:173] offset:7168
	v_cndmask_b32_e64 v130, v130, v168, s[12:13]
	v_mul_f32_e32 v168, 0x37800000, v130
	v_cndmask_b32_e32 v130, v130, v168, vcc
	v_cmp_class_f32_e32 vcc, v129, v194
	s_nop 1
	v_cndmask_b32_e32 v129, v130, v129, vcc
	v_div_scale_f32 v130, s[12:13], v129, v129, 1.0
	v_rcp_f32_e32 v168, v130
	s_nop 0
	v_fma_f32 v169, -v130, v168, 1.0
	v_fmac_f32_e32 v168, v169, v168
	v_div_scale_f32 v169, vcc, 1.0, v129, 1.0
	v_mul_f32_e32 v174, v169, v168
	v_fma_f32 v175, -v130, v174, v169
	v_fmac_f32_e32 v174, v175, v168
	v_fma_f32 v130, -v130, v174, v169
	v_div_fmas_f32 v130, v130, v168, v174
	v_div_fixup_f32 v130, v130, v129, 1.0
	v_pk_mul_f32 v[174:175], v[130:131], v[208:209] op_sel_hi:[0,1]
	v_mov_b32_e32 v129, 0
	v_cvt_pk_fp8_f32 v129, v174, v175
	v_pk_mul_f32 v[176:177], v[130:131], v[210:211] op_sel_hi:[0,1]
	v_mov_b32_e32 v168, v213
	v_mov_b32_e32 v169, v215
	v_cvt_pk_fp8_f32 v129, v176, v177 op_sel:[0,0,1]
	v_pk_mul_f32 v[180:181], v[130:131], v[168:169] op_sel_hi:[0,1]
	ds_write_b128 v196, v[174:177]
	v_pk_mul_f32 v[168:169], v[130:131], v[216:217] op_sel_hi:[0,1]
	global_store_dword v[166:167], v129, off
	v_mov_b32_e32 v129, 0
	v_pk_mul_f32 v[172:173], v[222:223], v[130:131] op_sel_hi:[1,0]
	v_mov_b32_e32 v176, 0
	v_cvt_pk_fp8_f32 v129, v168, v169
	v_cvt_pk_fp8_f32 v176, v172, v173
	v_mov_b32_e32 v213, v214
	v_pk_mul_f32 v[178:179], v[130:131], v[212:213] op_sel_hi:[0,1]
	v_pk_mul_f32 v[170:171], v[130:131], v[218:219] op_sel_hi:[0,1]
	v_pk_mul_f32 v[174:175], v[224:225], v[130:131] op_sel_hi:[1,0]
	v_cvt_pk_fp8_f32 v182, v178, v179
	v_cvt_pk_fp8_f32 v129, v170, v171 op_sel:[0,0,1]
	v_cvt_pk_fp8_f32 v176, v174, v175 op_sel:[0,0,1]
	ds_write_b128 v196, v[178:181] offset:1024
	ds_write_b128 v196, v[168:171] offset:2048
	v_mov_b32_e32 v168, v227
	v_mov_b32_e32 v169, v229
	v_mov_b32_e32 v227, v228
	v_mov_b32_e32 v178, v231
	v_mov_b32_e32 v231, v232
	v_cvt_pk_fp8_f32 v182, v180, v181 op_sel:[0,0,1]
	global_store_dword v[166:167], v129, off offset:512
	global_store_dword v[166:167], v176, off offset:768
	v_pk_mul_f32 v[170:171], v[130:131], v[168:169] op_sel_hi:[0,1]
	v_pk_mul_f32 v[168:169], v[130:131], v[226:227] op_sel_hi:[0,1]
	v_mov_b32_e32 v129, 0
	v_pk_mul_f32 v[176:177], v[130:131], v[230:231] op_sel_hi:[0,1]
	v_mov_b32_e32 v180, 0
	v_cvt_pk_fp8_f32 v129, v168, v169
	v_cvt_pk_fp8_f32 v180, v176, v177
	v_mov_b32_e32 v179, v233
	v_pk_mul_f32 v[178:179], v[130:131], v[178:179] op_sel_hi:[0,1]
	v_cvt_pk_fp8_f32 v129, v170, v171 op_sel:[0,0,1]
	v_cvt_pk_fp8_f32 v180, v178, v179 op_sel:[0,0,1]
	ds_write_b128 v196, v[172:175] offset:3072
	ds_write_b128 v196, v[168:171] offset:4096
	global_store_dword v[166:167], v129, off offset:1024
	global_store_dword v[166:167], v180, off offset:1280
	v_pk_mul_f32 v[168:169], v[130:131], v[234:235] op_sel_hi:[0,1]
	v_mov_b32_e32 v129, 0
	v_pk_mul_f32 v[172:173], v[240:241], v[130:131] op_sel_hi:[1,0]
	v_mov_b32_e32 v180, 0
	v_cvt_pk_fp8_f32 v129, v168, v169
	v_cvt_pk_fp8_f32 v180, v172, v173
	v_pk_mul_f32 v[170:171], v[130:131], v[236:237] op_sel_hi:[0,1]
	v_pk_mul_f32 v[174:175], v[242:243], v[130:131] op_sel_hi:[1,0]
	v_cvt_pk_fp8_f32 v129, v170, v171 op_sel:[0,0,1]
	v_cvt_pk_fp8_f32 v180, v174, v175 op_sel:[0,0,1]
	s_and_b64 vcc, exec, s[34:35]
	global_store_dword v[166:167], v182, off offset:256
	ds_write_b128 v196, v[176:179] offset:5120
	global_store_dword v[166:167], v129, off offset:1536
	ds_write_b128 v196, v[168:171] offset:6144
	global_store_dword v[166:167], v180, off offset:1792
	ds_write_b128 v196, v[172:175] offset:7168
	s_waitcnt lgkmcnt(0)
	s_barrier
	s_cbranch_vccnz .LBB0_975
	s_ashr_i32 s31, s30, 31
	s_lshl_b64 s[12:13], s[30:31], 16
	v_mbcnt_lo_u32_b32 v129, -1, 0
	v_mbcnt_hi_u32_b32 v129, -1, v129
	s_add_u32 s12, s1, s12
	v_lshlrev_b32_e32 v129, 3, v129
	s_addc_u32 s13, s2, s13
	v_and_b32_e32 v130, 0x7ffffff8, v129
	v_lshl_add_u64 v[132:133], s[12:13], 0, v[130:131]
	v_add_co_u32_e32 v148, vcc, s41, v132
	v_lshl_add_u64 v[160:161], v[132:133], 0, s[28:29]
	s_nop 0
	v_addc_co_u32_e32 v149, vcc, 0, v133, vcc
	global_load_dwordx2 v[132:133], v130, s[12:13]
	global_load_dwordx2 v[134:135], v130, s[12:13] offset:512
	global_load_dwordx2 v[140:141], v130, s[12:13] offset:1024
	global_load_dwordx2 v[144:145], v130, s[12:13] offset:1536
	global_load_dwordx2 v[136:137], v[160:161], off offset:512
	global_load_dwordx2 v[138:139], v[160:161], off offset:1024
	global_load_dwordx2 v[142:143], v[160:161], off offset:1536
	global_load_dwordx2 v[146:147], v[160:161], off offset:2048
	global_load_dwordx2 v[150:151], v130, s[12:13] offset:2048
	global_load_dwordx2 v[152:153], v130, s[12:13] offset:2560
	global_load_dwordx2 v[156:157], v130, s[12:13] offset:3072
	global_load_dwordx2 v[162:163], v130, s[12:13] offset:3584
	s_nop 0
	global_load_dwordx2 v[148:149], v[148:149], off
	s_nop 0
	global_load_dwordx2 v[154:155], v[160:161], off offset:2560
	global_load_dwordx2 v[158:159], v[160:161], off offset:3072
	s_nop 0
	global_load_dwordx2 v[160:161], v[160:161], off offset:3584
